# attention filler store: LDS transposer reads hoisted in front of the K/V tile loads (latency hidden), on top of v55
# speedup vs baseline: 1.0069x; 1.0069x over previous
; DEV int ltid() { int t = threadIdx.x; asm volatile("" : "+v"(t)); return t; }
; DEV void fill_store(CParams& p, int wg, int slot, int bufsel) {
;   extern __shared__ __attribute__((aligned(16))) char shm[];
;   const unsigned* T = (const unsigned*)(shm + FILL_LDS_OFF + bufsel * FILL_TB); const int tid = ltid(), nl = tid >> 3, cc = tid & 7;
;   const FillDesc d = fill_decode(p, wg, slot);
;   u32x4 v; v.x = T[nl * 33 + 4 * cc]; v.y = T[nl * 33 + 4 * cc + 1]; v.z = T[nl * 33 + 4 * cc + 2]; v.w = T[nl * 33 + 4 * cc + 3];
;   *(u32x4*)(d.dst + (long)perm_row(d.perm, d.n0 + nl) * 2048 + d.kh + 16 * cc) = v;
; }
.LBB0_898:
	s_xor_b32 s56, s36, 1
	s_mul_i32 s56, s56, 0x2200
	v_add_u32_e32 v76, s56, v244
	ds_read2_b32 v[72:73], v76 offset1:1
	ds_read2_b32 v[74:75], v76 offset0:2 offset1:3
	v_add_co_u32_e32 v68, vcc, 0xffffe000, v188
	s_nop 1
	v_addc_co_u32_e32 v69, vcc, -1, v189, vcc
	global_load_dwordx4 v[148:151], v[68:69], off
	global_load_dwordx4 v[152:155], v[188:189], off
	v_add_co_u32_e32 v68, vcc, 0xffffc000, v190
	s_nop 1
	v_addc_co_u32_e32 v69, vcc, -1, v191, vcc
	v_add_co_u32_e32 v70, vcc, 0xffffe000, v190
	s_nop 1
	v_addc_co_u32_e32 v71, vcc, -1, v191, vcc
	global_load_dwordx4 v[156:159], v[68:69], off
	global_load_dwordx4 v[160:163], v[70:71], off
	global_load_dwordx4 v[164:167], v[190:191], off
	s_add_i32 s35, s34, 1
	s_cmp_gt_u32 s35, 62
	s_cbranch_scc1 .LBB0_907
.LBB0_899:
	s_add_i32 s57, s37, 66
	s_cmp_gt_u32 s57, 0x7f
	s_cbranch_scc1 .Lfst_a_d
	s_lshr_b32 s58, s57, 2
	s_lshl_b32 s58, s58, 23
	s_and_b32 s59, s57, 3
	s_lshl_b32 s59, s59, 9
	s_or_b32 s58, s58, s59
	s_add_u32 s60, s12, s58
	s_addc_u32 s61, s13, 0
	s_waitcnt lgkmcnt(0)
	global_store_dwordx4 v246, v[72:75], s[60:61]
	s_branch .Lfst_a_end
.Lfst_a_d:
	s_sub_u32 s57, s57, 0x80
	s_lshr_b32 s58, s57, 1
	s_lshl_b32 s58, s58, 22
	s_and_b32 s59, s57, 1
	s_lshl_b32 s59, s59, 10
	s_or_b32 s58, s58, s59
	s_add_u32 s60, s14, s58
	s_addc_u32 s61, s15, 0
	s_waitcnt lgkmcnt(0)
	global_store_dwordx4 v247, v[72:75], s[60:61]

; DEV int ltid() { int t = threadIdx.x; asm volatile("" : "+v"(t)); return t; }
; DEV void fill_store(CParams& p, int wg, int slot, int bufsel) {
;   extern __shared__ __attribute__((aligned(16))) char shm[];
;   const unsigned* T = (const unsigned*)(shm + FILL_LDS_OFF + bufsel * FILL_TB); const int tid = ltid(), nl = tid >> 3, cc = tid & 7;
;   const FillDesc d = fill_decode(p, wg, slot);
;   u32x4 v; v.x = T[nl * 33 + 4 * cc]; v.y = T[nl * 33 + 4 * cc + 1]; v.z = T[nl * 33 + 4 * cc + 2]; v.w = T[nl * 33 + 4 * cc + 3];
;   *(u32x4*)(d.dst + (long)perm_row(d.perm, d.n0 + nl) * 2048 + d.kh + 16 * cc) = v;
; }
.LBB0_1105:
	s_xor_b32 s56, s37, 1
	s_mul_i32 s56, s56, 0x2200
	v_add_u32_e32 v76, s56, v244
	ds_read2_b32 v[72:73], v76 offset1:1
	ds_read2_b32 v[74:75], v76 offset0:2 offset1:3
	v_add_co_u32_e32 v68, vcc, 0xffffe000, v188
	s_nop 1
	v_addc_co_u32_e32 v69, vcc, -1, v189, vcc
	global_load_dwordx4 v[148:151], v[68:69], off
	global_load_dwordx4 v[152:155], v[188:189], off
	v_add_co_u32_e32 v68, vcc, 0xffffc000, v190
	s_nop 1
	v_addc_co_u32_e32 v69, vcc, -1, v191, vcc
	v_add_co_u32_e32 v70, vcc, 0xffffe000, v190
	s_nop 1
	v_addc_co_u32_e32 v71, vcc, -1, v191, vcc
	global_load_dwordx4 v[156:159], v[68:69], off
	global_load_dwordx4 v[160:163], v[70:71], off
	global_load_dwordx4 v[164:167], v[190:191], off
	s_add_i32 s36, s35, 1
	s_cmp_gt_u32 s36, 61
	s_cbranch_scc1 .LBB0_1114
.LBB0_1106:
	s_add_i32 s57, s38, 129
	s_sub_u32 s57, s57, 0x80
	s_lshr_b32 s58, s57, 1
	s_lshl_b32 s58, s58, 22
	s_and_b32 s59, s57, 1
	s_lshl_b32 s59, s59, 10
	s_or_b32 s58, s58, s59
	s_add_u32 s60, s14, s58
	s_addc_u32 s61, s15, 0
	s_waitcnt lgkmcnt(0)
	global_store_dwordx4 v247, v[72:75], s[60:61]
